# baseline (speedup 1.0000x reference)
_Z11proj_kernelPKfS0_S0_PKDF16_S0_S0_S0_PDF16_S3_S3_Pj:
	s_ashr_i32 s12, s2, 6
	s_load_dwordx8 s[4:11], s[0:1], 0x0
	s_load_dwordx4 s[56:59], s[0:1], 0x20
	s_load_dwordx2 s[60:61], s[0:1], 0x30
	s_cmp_gt_u32 s2, 63
	s_cselect_b64 s[22:23], -1, 0
	s_cmp_lg_u32 s12, 1
	s_cselect_b64 s[18:19], -1, 0
	s_cmp_eq_u32 s12, 1
	s_cselect_b64 s[20:21], -1, 0
	s_and_b64 s[14:15], s[20:21], exec
	s_waitcnt lgkmcnt(0)
	s_cselect_b32 s14, s6, s8
	s_cselect_b32 s15, s7, s9
	s_ashr_i32 s13, s12, 31
	s_lshl_b32 s28, s2, 7
	s_lshl_b64 s[6:7], s[12:13], 19
	s_and_b32 s3, s28, 0x1f80
	s_cmp_lt_u32 s2, 64
	s_cselect_b64 vcc, -1, 0
	v_lshrrev_b32_e32 v1, 2, v0
	v_or_b32_e32 v2, s3, v1
	s_and_b64 s[8:9], vcc, exec
	s_cselect_b32 s25, s5, s15
	s_cselect_b32 s24, s4, s14
	s_cmp_eq_u32 s12, 1
	s_cselect_b32 s62, s58, s60
	s_cselect_b32 s63, s59, s61
	s_cmp_lt_u32 s2, 64
	s_cselect_b32 s62, s56, s62
	s_cselect_b32 s63, s57, s63
	v_and_b32_e32 v253, 0xff, v0
	v_lshlrev_b32_e32 v253, 3, v253
	v_lshlrev_b32_e32 v2, 11, v2
	v_mov_b32_e32 v3, 0
	v_lshlrev_b32_e32 v6, 5, v0
	s_add_u32 s4, s10, s6
	v_lshl_add_u64 v[4:5], s[24:25], 0, v[2:3]
	v_and_b32_e32 v6, 0x60, v6
	v_mov_b32_e32 v7, v3
	v_lshlrev_b32_e32 v56, 4, v0
	v_mov_b32_e32 v57, v3
	s_addc_u32 s5, s11, s7
	v_lshl_add_u64 v[4:5], v[4:5], 0, v[6:7]
	s_movk_i32 s8, 0x2000
	v_lshl_add_u64 v[6:7], s[4:5], 0, v[56:57]
	global_load_dword v254, v253, s[62:63]
	global_load_dwordx4 v[8:11], v[4:5], off nt
	global_load_dwordx4 v[12:15], v[4:5], off offset:16 nt
	global_load_dwordx4 v[16:19], v56, s[4:5]
	v_add_co_u32_e64 v28, s[4:5], s8, v6
	s_mov_b32 s33, 0xa000
	s_nop 0
	v_addc_co_u32_e64 v29, s[4:5], 0, v7, s[4:5]
	s_movk_i32 s4, 0x4000
	s_nop 0
	v_add_co_u32_e64 v30, s[4:5], s4, v6
	s_mov_b32 s6, 0xe000
	s_nop 0
	v_addc_co_u32_e64 v31, s[4:5], 0, v7, s[4:5]
	global_load_dwordx4 v[20:23], v[28:29], off
	global_load_dwordx4 v[24:27], v[30:31], off
	s_movk_i32 s4, 0x6000
	v_add_co_u32_e64 v40, s[4:5], s4, v6
	v_lshlrev_b32_e32 v57, 6, v1
	s_nop 0
	v_addc_co_u32_e64 v41, s[4:5], 0, v7, s[4:5]
	global_load_dwordx4 v[28:31], v[40:41], off
	global_load_dwordx4 v[32:35], v[4:5], off offset:128 nt
	global_load_dwordx4 v[36:39], v[4:5], off offset:144 nt
	s_mov_b32 s4, 0x8000
	v_add_co_u32_e64 v40, s[4:5], s4, v6
	v_bitop3_b32 v58, v56, 48, v0 bitop3:0x48
	s_nop 0
	v_addc_co_u32_e64 v41, s[4:5], 0, v7, s[4:5]
	v_add_co_u32_e64 v44, s[4:5], s33, v6
	global_load_dwordx4 v[40:43], v[40:41], off
	s_nop 0
	v_addc_co_u32_e64 v45, s[4:5], 0, v7, s[4:5]
	s_mov_b32 s4, 0xc000
	s_nop 0
	v_add_co_u32_e64 v48, s[4:5], s4, v6
	global_load_dwordx4 v[44:47], v[44:45], off
	s_nop 0
	v_addc_co_u32_e64 v49, s[4:5], 0, v7, s[4:5]
	v_add_co_u32_e64 v52, s[4:5], s6, v6
	global_load_dwordx4 v[48:51], v[48:49], off
	s_nop 0
	v_addc_co_u32_e64 v53, s[4:5], 0, v7, s[4:5]
	global_load_dwordx4 v[52:55], v[52:53], off
	s_mov_b32 s4, 0x1e000
	v_add3_u32 v209, 0, v57, v58
	v_add_u32_e32 v208, 0, v56
	v_readfirstlane_b32 s30, v0
	v_bfe_u32 v207, v0, 5, 1
	v_bitop3_b32 v1, v207, v1, 3 bitop3:0x78
	v_lshlrev_b32_e32 v210, 4, v1
	s_mov_b32 s34, 0x14000
	v_add_u32_e32 v213, 0x2000, v208
	s_mov_b32 s43, 0
	s_lshr_b32 s29, s30, 6
	s_mov_b32 s35, -2
	s_mov_b32 s36, 0xffff2000
	s_mov_b32 s37, 0xffff4000
	s_mov_b32 s38, 0xffff6000
	s_movk_i32 s39, 0x8000
	s_movk_i32 s40, 0xa000
	s_movk_i32 s41, 0xc000
	s_movk_i32 s42, 0xe000
	s_mov_b64 s[26:27], 0x100
	v_mov_b32_e32 v56, v3
	v_mov_b32_e32 v57, v3
	v_mov_b32_e32 v58, v3
	v_mov_b32_e32 v59, v3
	v_mov_b32_e32 v60, v3
	v_mov_b32_e32 v61, v3
	v_mov_b32_e32 v62, v3
	v_mov_b32_e32 v63, v3
	v_mov_b32_e32 v64, v3
	v_mov_b32_e32 v65, v3
	v_mov_b32_e32 v66, v3
	v_mov_b32_e32 v67, v3
	v_mov_b32_e32 v68, v3
	v_mov_b32_e32 v69, v3
	v_mov_b32_e32 v70, v3
	s_waitcnt vmcnt(11)
	v_cvt_pk_f16_f32 v8, v8, v9
	v_cvt_pk_f16_f32 v9, v10, v11
	s_waitcnt vmcnt(10)
	v_cvt_pk_f16_f32 v10, v12, v13
	v_cvt_pk_f16_f32 v11, v14, v15
	ds_write_b128 v209, v[8:11]
	v_and_b32_e32 v10, 31, v0
	s_waitcnt vmcnt(9)
	ds_write_b128 v208, v[16:19] offset:8192
	s_waitcnt vmcnt(8)
	ds_write_b128 v208, v[20:23] offset:16384
	s_waitcnt vmcnt(7)
	ds_write_b128 v208, v[24:27] offset:24576
	s_load_dwordx2 s[16:17], s[0:1], 0x50
	s_load_dwordx4 s[12:15], s[0:1], 0x40
	s_load_dwordx8 s[4:11], s[0:1], 0x20
	s_lshl_b32 s0, s30, 1
	s_and_b32 s31, s0, 0x180
	s_lshr_b32 s0, s30, 2
	v_bfe_u32 v11, v0, 2, 2
	s_and_b32 s0, s0, 0x3fffffc0
	s_waitcnt vmcnt(5)
	v_cvt_pk_f16_f32 v8, v32, v33
	v_cvt_pk_f16_f32 v9, v34, v35
	v_or_b32_e32 v12, s31, v10
	v_or_b32_e32 v206, s0, v10
	v_bitop3_b32 v1, v207, v11, 2 bitop3:0x36
	s_waitcnt vmcnt(4)
	v_cvt_pk_f16_f32 v10, v36, v37
	v_cvt_pk_f16_f32 v11, v38, v39
	s_mov_b32 s0, 0x10000
	ds_write_b128 v208, v[28:31] offset:32768
	ds_write_b128 v209, v[8:11] offset:40960
	v_add_co_u32_e64 v8, s[0:1], s0, v6
	global_load_dwordx4 v[154:157], v[4:5], off offset:272 nt
	global_load_dwordx4 v[162:165], v[4:5], off offset:256 nt
	v_addc_co_u32_e64 v9, s[0:1], 0, v7, s[0:1]
	s_mov_b32 s0, 0x12000
	global_load_dwordx4 v[158:161], v[8:9], off
	v_add_co_u32_e64 v8, s[0:1], s0, v6
	v_lshl_add_u32 v211, v12, 6, 0
	s_nop 0
	v_addc_co_u32_e64 v9, s[0:1], 0, v7, s[0:1]
	v_add_co_u32_e64 v10, s[0:1], s34, v6
	v_add_u32_e32 v14, 0x12000, v208
	s_nop 0
	v_addc_co_u32_e64 v11, s[0:1], 0, v7, s[0:1]
	s_mov_b32 s0, 0x16000
	s_nop 0
	v_add_co_u32_e64 v12, s[0:1], s0, v6
	s_waitcnt vmcnt(3)
	ds_write_b128 v14, v[52:55]
	v_addc_co_u32_e64 v13, s[0:1], 0, v7, s[0:1]
	s_mov_b32 s0, 0x18000
	s_nop 0
	v_add_co_u32_e64 v14, s[0:1], s0, v6
	ds_write_b128 v208, v[40:43] offset:49152
	s_nop 0
	v_addc_co_u32_e64 v15, s[0:1], 0, v7, s[0:1]
	s_mov_b32 s0, 0x1a000
	s_nop 0
	v_add_co_u32_e64 v16, s[0:1], s0, v6
	ds_write_b128 v208, v[44:47] offset:57344
	s_nop 0
	v_addc_co_u32_e64 v17, s[0:1], 0, v7, s[0:1]
	s_mov_b32 s0, 0x1c000
	ds_write_b128 v213, v[48:51] offset:57344
	v_add_co_u32_e64 v18, s[0:1], s0, v6
	v_add_u32_e32 v216, v211, v210
	s_nop 0
	v_addc_co_u32_e64 v19, s[0:1], 0, v7, s[0:1]
	global_load_dwordx4 v[174:177], v[8:9], off
	global_load_dwordx4 v[166:169], v[10:11], off
	global_load_dwordx4 v[170:173], v[12:13], off
	global_load_dwordx4 v[142:145], v[4:5], off offset:400 nt
	global_load_dwordx4 v[150:153], v[4:5], off offset:384 nt
	global_load_dwordx4 v[138:141], v[14:15], off
	global_load_dwordx4 v[146:149], v[16:17], off
	global_load_dwordx4 v[134:137], v[18:19], off
	s_mov_b32 s0, 0x1e000
	v_add_co_u32_e64 v8, s[0:1], s0, v6
	s_nop 1
	v_addc_co_u32_e64 v9, s[0:1], 0, v7, s[0:1]
	global_load_dwordx4 v[130:133], v[8:9], off
	s_waitcnt lgkmcnt(0)
	s_barrier
	v_lshl_add_u32 v218, v206, 6, 0
	v_add_u32_e32 v217, v218, v210
	ds_read_b128 v[198:201], v216 offset:8192
	ds_read_b128 v[194:197], v216 offset:10240
	ds_read_b128 v[190:193], v216 offset:12288
	ds_read_b128 v[178:181], v216 offset:14336
	ds_read_b128 v[186:189], v217
	ds_read_b128 v[182:185], v217 offset:2048
	v_and_b32_e32 v20, 3, v0
	v_lshl_or_b32 v2, v20, 5, v2
	s_mov_b64 s[0:1], 0x2e000
	v_lshlrev_b32_e32 v212, 4, v1
	v_lshl_add_u64 v[202:203], v[6:7], 0, s[0:1]
	s_mov_b64 s[0:1], 0x290
	v_lshl_add_u64 v[4:5], s[24:25], 0, v[2:3]
	v_lshl_add_u64 v[204:205], v[4:5], 0, s[0:1]
	s_mov_b64 s[24:25], 0x10000
	v_mov_b32_e32 v2, v3
	v_mov_b32_e32 v4, v3
	v_mov_b32_e32 v5, v3
	v_mov_b32_e32 v6, v3
	v_mov_b32_e32 v7, v3
	v_mov_b32_e32 v8, v3
	v_mov_b32_e32 v9, v3
	v_mov_b32_e32 v10, v3
	v_mov_b32_e32 v11, v3
	v_mov_b32_e32 v12, v3
	v_mov_b32_e32 v13, v3
	v_mov_b32_e32 v14, v3
	v_mov_b32_e32 v15, v3
	v_mov_b32_e32 v16, v3
	v_mov_b32_e32 v17, v3
	v_mov_b32_e32 v18, v3
	v_mov_b32_e32 v19, v3
	v_mov_b32_e32 v20, v3
	v_mov_b32_e32 v21, v3
	v_mov_b32_e32 v22, v3
	v_mov_b32_e32 v23, v3
	v_mov_b32_e32 v24, v3
	v_mov_b32_e32 v25, v3
	v_mov_b32_e32 v26, v3
	v_mov_b32_e32 v27, v3
	v_mov_b32_e32 v28, v3
	v_mov_b32_e32 v29, v3
	v_mov_b32_e32 v30, v3
	v_mov_b32_e32 v31, v3
	v_mov_b32_e32 v32, v3
	v_mov_b32_e32 v33, v3
	v_mov_b32_e32 v34, v3
	v_mov_b32_e32 v35, v3
	v_mov_b32_e32 v36, v3
	v_mov_b32_e32 v37, v3
	v_mov_b32_e32 v38, v3
	v_mov_b32_e32 v39, v3
	v_mov_b32_e32 v40, v3
	v_mov_b32_e32 v41, v3
	v_mov_b32_e32 v42, v3
	v_mov_b32_e32 v43, v3
	v_mov_b32_e32 v44, v3
	v_mov_b32_e32 v45, v3
	v_mov_b32_e32 v46, v3
	v_mov_b32_e32 v47, v3
	v_mov_b32_e32 v48, v3
	v_mov_b32_e32 v49, v3
	v_mov_b32_e32 v50, v3
	v_mov_b32_e32 v51, v3
	v_mov_b32_e32 v52, v3
	v_mov_b32_e32 v53, v3
	v_mov_b32_e32 v54, v3
	v_mov_b32_e32 v55, v3
	v_mov_b32_e32 v71, v3
	v_mov_b32_e32 v72, v3
	v_mov_b32_e32 v73, v3
	v_mov_b32_e32 v74, v3
	v_mov_b32_e32 v75, v3
	v_mov_b32_e32 v76, v3
	v_mov_b32_e32 v77, v3
	v_mov_b32_e32 v78, v3
	v_mov_b32_e32 v79, v3
	v_mov_b32_e32 v80, v3
	v_mov_b32_e32 v81, v3
	v_mov_b32_e32 v82, v3
	v_mov_b32_e32 v83, v3
	v_mov_b32_e32 v84, v3
	v_mov_b32_e32 v85, v3
	v_mov_b32_e32 v86, v3
	v_mov_b32_e32 v87, v3
	v_mov_b32_e32 v88, v3
	v_mov_b32_e32 v89, v3
	v_mov_b32_e32 v90, v3
	v_mov_b32_e32 v91, v3
	v_mov_b32_e32 v92, v3
	v_mov_b32_e32 v93, v3
	v_mov_b32_e32 v94, v3
	v_mov_b32_e32 v95, v3
	v_mov_b32_e32 v96, v3
	v_mov_b32_e32 v97, v3
	v_mov_b32_e32 v98, v3
	v_mov_b32_e32 v99, v3
	v_mov_b32_e32 v100, v3
	v_mov_b32_e32 v101, v3
	v_mov_b32_e32 v102, v3
	v_mov_b32_e32 v103, v3
	v_mov_b32_e32 v104, v3
	v_mov_b32_e32 v105, v3
	v_mov_b32_e32 v106, v3
	v_mov_b32_e32 v107, v3
	v_mov_b32_e32 v108, v3
	v_mov_b32_e32 v109, v3
	v_mov_b32_e32 v110, v3
	v_mov_b32_e32 v111, v3
	v_mov_b32_e32 v112, v3
	v_mov_b32_e32 v113, v3
	v_mov_b32_e32 v114, v3
	v_mov_b32_e32 v115, v3
	v_mov_b32_e32 v116, v3
	v_mov_b32_e32 v117, v3
	v_mov_b32_e32 v118, v3
	v_mov_b32_e32 v119, v3
	v_mov_b32_e32 v120, v3
	v_mov_b32_e32 v121, v3
	v_mov_b32_e32 v122, v3
	v_mov_b32_e32 v123, v3
	v_mov_b32_e32 v124, v3
	v_mov_b32_e32 v125, v3
	v_mov_b32_e32 v126, v3
	v_mov_b32_e32 v127, v3
	v_mov_b32_e32 v128, v3
	v_mov_b32_e32 v129, v3
	v_and_b32_e32 v1, 63, v0
	v_add_u32_e32 v215, v211, v212
	v_add_u32_e32 v214, v218, v212

.LBB1_9:
	s_andn2_b64 vcc, exec, s[4:5]
	s_cbranch_vccnz .LBB1_13
	v_lshl_or_b32 v2, s9, 6, v1
	s_movk_i32 s13, 0x410
	v_mul_lo_u32 v2, v2, s13
	v_add_u32_e32 v22, 0, v2
	s_and_b32 s12, s12, 6
	v_lshl_add_u32 v23, s12, 7, v22
	s_lshl_b32 s2, s12, 5
	ds_read_b128 v[2:5], v23
	ds_read_b128 v[6:9], v23 offset:16
	ds_read_b128 v[10:13], v23 offset:32
	ds_read_b128 v[14:17], v23 offset:48
	s_mov_b32 s3, 0
	s_add_i32 s2, s2, s9
	s_lshl_b64 s[4:5], s[2:3], 13
	s_add_u32 s4, s7, s4
	s_addc_u32 s5, s8, s5
	v_lshlrev_b32_e32 v18, 4, v1
	s_waitcnt lgkmcnt(3)
	global_store_dwordx4 v18, v[2:5], s[4:5] sc1
	s_waitcnt lgkmcnt(2)
	global_store_dwordx4 v18, v[6:9], s[4:5] offset:1024 sc1
	s_waitcnt lgkmcnt(1)
	global_store_dwordx4 v18, v[10:13], s[4:5] offset:2048 sc1
	s_waitcnt lgkmcnt(0)
	global_store_dwordx4 v18, v[14:17], s[4:5] offset:3072 sc1
	ds_read_b128 v[2:5], v23 offset:64
	ds_read_b128 v[6:9], v23 offset:80
	ds_read_b128 v[10:13], v23 offset:96
	ds_read_b128 v[14:17], v23 offset:112
	v_mov_b32_e32 v19, 0
	v_lshl_add_u64 v[20:21], s[4:5], 0, v[18:19]
	s_movk_i32 s4, 0x1000
	v_add_co_u32_e32 v20, vcc, s4, v20
	s_or_b32 s2, s12, 1
	s_nop 0
	v_addc_co_u32_e32 v21, vcc, 0, v21, vcc
	s_waitcnt lgkmcnt(3)
	global_store_dwordx4 v[20:21], v[2:5], off sc1
	s_waitcnt lgkmcnt(2)
	global_store_dwordx4 v[20:21], v[6:9], off offset:1024 sc1
	s_waitcnt lgkmcnt(1)
	global_store_dwordx4 v[20:21], v[10:13], off offset:2048 sc1
	s_waitcnt lgkmcnt(0)
	global_store_dwordx4 v[20:21], v[14:17], off offset:3072 sc1
	v_lshl_add_u32 v22, s2, 7, v22
	s_lshl_b32 s2, s2, 5
	ds_read_b128 v[2:5], v22
	ds_read_b128 v[6:9], v22 offset:16
	ds_read_b128 v[10:13], v22 offset:32
	ds_read_b128 v[14:17], v22 offset:48
	s_add_i32 s2, s2, s9
	s_lshl_b64 s[2:3], s[2:3], 13
	s_add_u32 s2, s7, s2
	s_addc_u32 s3, s8, s3
	s_waitcnt lgkmcnt(3)
	global_store_dwordx4 v18, v[2:5], s[2:3] sc1
	s_waitcnt lgkmcnt(2)
	global_store_dwordx4 v18, v[6:9], s[2:3] offset:1024 sc1
	s_waitcnt lgkmcnt(1)
	global_store_dwordx4 v18, v[10:13], s[2:3] offset:2048 sc1
	s_waitcnt lgkmcnt(0)
	global_store_dwordx4 v18, v[14:17], s[2:3] offset:3072 sc1
	ds_read_b128 v[2:5], v22 offset:64
	ds_read_b128 v[6:9], v22 offset:80
	ds_read_b128 v[10:13], v22 offset:96
	ds_read_b128 v[14:17], v22 offset:112
	v_lshl_add_u64 v[20:21], s[2:3], 0, v[18:19]
	v_add_co_u32_e32 v18, vcc, s4, v20
	s_nop 1
	v_addc_co_u32_e32 v19, vcc, 0, v21, vcc
	s_waitcnt lgkmcnt(3)
	global_store_dwordx4 v[18:19], v[2:5], off sc1
	s_waitcnt lgkmcnt(2)
	global_store_dwordx4 v[18:19], v[6:9], off offset:1024 sc1
	s_waitcnt lgkmcnt(1)
	global_store_dwordx4 v[18:19], v[10:13], off offset:2048 sc1
	s_waitcnt lgkmcnt(0)
	global_store_dwordx4 v[18:19], v[14:17], off offset:3072 sc1
	v_and_b32_e32 v2, 7, v0
	v_lshl_add_u32 v18, v2, 7, 0
	v_lshl_add_u32 v6, v2, 2, 0
	v_lshrrev_b32_e32 v2, 3, v0
	v_mad_u32_u24 v19, v2, s13, v18
	ds_read_b128 v[2:5], v19
	v_add_u32_e32 v20, 0x20800, v6
	ds_read_b128 v[6:9], v19 offset:16
	ds_read_b128 v[10:13], v19 offset:32
	ds_read_b128 v[14:17], v19 offset:48
	ds_read_b128 v[28:31], v19 offset:64
	ds_read_b128 v[32:35], v19 offset:80
	ds_read_b128 v[36:39], v19 offset:96
	ds_read_b128 v[40:43], v19 offset:112
	v_or_b32_e32 v21, 0x200, v0
	v_lshrrev_b32_e32 v21, 3, v21
	v_mad_u32_u24 v18, v21, s13, v18
	ds_read_b128 v[44:47], v18
	ds_read_b128 v[48:51], v18 offset:16
	ds_read_b128 v[52:55], v18 offset:32
	ds_read_b128 v[56:59], v18 offset:48
	s_waitcnt lgkmcnt(8)
	v_fma_mix_f32 v24, v2, v2, 0 op_sel_hi:[1,1,0]
	v_fma_mix_f32 v25, v6, v6, 0 op_sel_hi:[1,1,0]
	v_fma_mix_f32 v26, v10, v10, 0 op_sel_hi:[1,1,0]
	v_fma_mix_f32 v27, v14, v14, 0 op_sel_hi:[1,1,0]
	v_fma_mix_f32 v24, v2, v2, v24 op_sel:[1,1,0] op_sel_hi:[1,1,0]
	v_fma_mix_f32 v25, v6, v6, v25 op_sel:[1,1,0] op_sel_hi:[1,1,0]
	v_fma_mix_f32 v26, v10, v10, v26 op_sel:[1,1,0] op_sel_hi:[1,1,0]
	v_fma_mix_f32 v27, v14, v14, v27 op_sel:[1,1,0] op_sel_hi:[1,1,0]
	v_fma_mix_f32 v24, v3, v3, v24 op_sel_hi:[1,1,0]
	v_fma_mix_f32 v25, v7, v7, v25 op_sel_hi:[1,1,0]
	v_fma_mix_f32 v26, v11, v11, v26 op_sel_hi:[1,1,0]
	v_fma_mix_f32 v27, v15, v15, v27 op_sel_hi:[1,1,0]
	v_fma_mix_f32 v24, v3, v3, v24 op_sel:[1,1,0] op_sel_hi:[1,1,0]
	v_fma_mix_f32 v25, v7, v7, v25 op_sel:[1,1,0] op_sel_hi:[1,1,0]
	v_fma_mix_f32 v26, v11, v11, v26 op_sel:[1,1,0] op_sel_hi:[1,1,0]
	v_fma_mix_f32 v27, v15, v15, v27 op_sel:[1,1,0] op_sel_hi:[1,1,0]
	v_fma_mix_f32 v24, v4, v4, v24 op_sel_hi:[1,1,0]
	v_fma_mix_f32 v25, v8, v8, v25 op_sel_hi:[1,1,0]
	v_fma_mix_f32 v26, v12, v12, v26 op_sel_hi:[1,1,0]
	v_fma_mix_f32 v27, v16, v16, v27 op_sel_hi:[1,1,0]
	v_fma_mix_f32 v24, v4, v4, v24 op_sel:[1,1,0] op_sel_hi:[1,1,0]
	v_fma_mix_f32 v25, v8, v8, v25 op_sel:[1,1,0] op_sel_hi:[1,1,0]
	v_fma_mix_f32 v26, v12, v12, v26 op_sel:[1,1,0] op_sel_hi:[1,1,0]
	v_fma_mix_f32 v27, v16, v16, v27 op_sel:[1,1,0] op_sel_hi:[1,1,0]
	v_fma_mix_f32 v24, v5, v5, v24 op_sel_hi:[1,1,0]
	v_fma_mix_f32 v25, v9, v9, v25 op_sel_hi:[1,1,0]
	v_fma_mix_f32 v26, v13, v13, v26 op_sel_hi:[1,1,0]
	v_fma_mix_f32 v27, v17, v17, v27 op_sel_hi:[1,1,0]
	v_fma_mix_f32 v24, v5, v5, v24 op_sel:[1,1,0] op_sel_hi:[1,1,0]
	v_fma_mix_f32 v25, v9, v9, v25 op_sel:[1,1,0] op_sel_hi:[1,1,0]
	v_fma_mix_f32 v26, v13, v13, v26 op_sel:[1,1,0] op_sel_hi:[1,1,0]
	v_fma_mix_f32 v27, v17, v17, v27 op_sel:[1,1,0] op_sel_hi:[1,1,0]
	ds_read_b128 v[60:63], v18 offset:64
	ds_read_b128 v[64:67], v18 offset:80
	ds_read_b128 v[68:71], v18 offset:96
	ds_read_b128 v[72:75], v18 offset:112
	s_waitcnt lgkmcnt(8)
	v_fma_mix_f32 v24, v28, v28, v24 op_sel_hi:[1,1,0]
	v_fma_mix_f32 v25, v32, v32, v25 op_sel_hi:[1,1,0]
	v_fma_mix_f32 v26, v36, v36, v26 op_sel_hi:[1,1,0]
	v_fma_mix_f32 v27, v40, v40, v27 op_sel_hi:[1,1,0]
	v_fma_mix_f32 v24, v28, v28, v24 op_sel:[1,1,0] op_sel_hi:[1,1,0]
	v_fma_mix_f32 v25, v32, v32, v25 op_sel:[1,1,0] op_sel_hi:[1,1,0]
	v_fma_mix_f32 v26, v36, v36, v26 op_sel:[1,1,0] op_sel_hi:[1,1,0]
	v_fma_mix_f32 v27, v40, v40, v27 op_sel:[1,1,0] op_sel_hi:[1,1,0]
	v_fma_mix_f32 v24, v29, v29, v24 op_sel_hi:[1,1,0]
	v_fma_mix_f32 v25, v33, v33, v25 op_sel_hi:[1,1,0]
	v_fma_mix_f32 v26, v37, v37, v26 op_sel_hi:[1,1,0]
	v_fma_mix_f32 v27, v41, v41, v27 op_sel_hi:[1,1,0]
	v_fma_mix_f32 v24, v29, v29, v24 op_sel:[1,1,0] op_sel_hi:[1,1,0]
	v_fma_mix_f32 v25, v33, v33, v25 op_sel:[1,1,0] op_sel_hi:[1,1,0]
	v_fma_mix_f32 v26, v37, v37, v26 op_sel:[1,1,0] op_sel_hi:[1,1,0]
	v_fma_mix_f32 v27, v41, v41, v27 op_sel:[1,1,0] op_sel_hi:[1,1,0]
	v_fma_mix_f32 v24, v30, v30, v24 op_sel_hi:[1,1,0]
	v_fma_mix_f32 v25, v34, v34, v25 op_sel_hi:[1,1,0]
	v_fma_mix_f32 v26, v38, v38, v26 op_sel_hi:[1,1,0]
	v_fma_mix_f32 v27, v42, v42, v27 op_sel_hi:[1,1,0]
	v_fma_mix_f32 v24, v30, v30, v24 op_sel:[1,1,0] op_sel_hi:[1,1,0]
	v_fma_mix_f32 v25, v34, v34, v25 op_sel:[1,1,0] op_sel_hi:[1,1,0]
	v_fma_mix_f32 v26, v38, v38, v26 op_sel:[1,1,0] op_sel_hi:[1,1,0]
	v_fma_mix_f32 v27, v42, v42, v27 op_sel:[1,1,0] op_sel_hi:[1,1,0]
	v_fma_mix_f32 v24, v31, v31, v24 op_sel_hi:[1,1,0]
	v_fma_mix_f32 v25, v35, v35, v25 op_sel_hi:[1,1,0]
	v_fma_mix_f32 v26, v39, v39, v26 op_sel_hi:[1,1,0]
	v_fma_mix_f32 v27, v43, v43, v27 op_sel_hi:[1,1,0]
	v_fma_mix_f32 v24, v31, v31, v24 op_sel:[1,1,0] op_sel_hi:[1,1,0]
	v_fma_mix_f32 v25, v35, v35, v25 op_sel:[1,1,0] op_sel_hi:[1,1,0]
	v_fma_mix_f32 v26, v39, v39, v26 op_sel:[1,1,0] op_sel_hi:[1,1,0]
	v_fma_mix_f32 v27, v43, v43, v27 op_sel:[1,1,0] op_sel_hi:[1,1,0]
	v_add_f32_e32 v24, v24, v25
	v_add_f32_e32 v26, v26, v27
	s_nop 0
	v_add_f32_e32 v24, v24, v26
	s_nop 0
	ds_max_u32 v20, v24
	s_waitcnt lgkmcnt(5)
	v_fma_mix_f32 v24, v44, v44, 0 op_sel_hi:[1,1,0]
	v_fma_mix_f32 v25, v48, v48, 0 op_sel_hi:[1,1,0]
	v_fma_mix_f32 v26, v52, v52, 0 op_sel_hi:[1,1,0]
	v_fma_mix_f32 v27, v56, v56, 0 op_sel_hi:[1,1,0]
	v_fma_mix_f32 v24, v44, v44, v24 op_sel:[1,1,0] op_sel_hi:[1,1,0]
	v_fma_mix_f32 v25, v48, v48, v25 op_sel:[1,1,0] op_sel_hi:[1,1,0]
	v_fma_mix_f32 v26, v52, v52, v26 op_sel:[1,1,0] op_sel_hi:[1,1,0]
	v_fma_mix_f32 v27, v56, v56, v27 op_sel:[1,1,0] op_sel_hi:[1,1,0]
	v_fma_mix_f32 v24, v45, v45, v24 op_sel_hi:[1,1,0]
	v_fma_mix_f32 v25, v49, v49, v25 op_sel_hi:[1,1,0]
	v_fma_mix_f32 v26, v53, v53, v26 op_sel_hi:[1,1,0]
	v_fma_mix_f32 v27, v57, v57, v27 op_sel_hi:[1,1,0]
	v_fma_mix_f32 v24, v45, v45, v24 op_sel:[1,1,0] op_sel_hi:[1,1,0]
	v_fma_mix_f32 v25, v49, v49, v25 op_sel:[1,1,0] op_sel_hi:[1,1,0]
	v_fma_mix_f32 v26, v53, v53, v26 op_sel:[1,1,0] op_sel_hi:[1,1,0]
	v_fma_mix_f32 v27, v57, v57, v27 op_sel:[1,1,0] op_sel_hi:[1,1,0]
	v_fma_mix_f32 v24, v46, v46, v24 op_sel_hi:[1,1,0]
	v_fma_mix_f32 v25, v50, v50, v25 op_sel_hi:[1,1,0]
	v_fma_mix_f32 v26, v54, v54, v26 op_sel_hi:[1,1,0]
	v_fma_mix_f32 v27, v58, v58, v27 op_sel_hi:[1,1,0]
	v_fma_mix_f32 v24, v46, v46, v24 op_sel:[1,1,0] op_sel_hi:[1,1,0]
	v_fma_mix_f32 v25, v50, v50, v25 op_sel:[1,1,0] op_sel_hi:[1,1,0]
	v_fma_mix_f32 v26, v54, v54, v26 op_sel:[1,1,0] op_sel_hi:[1,1,0]
	v_fma_mix_f32 v27, v58, v58, v27 op_sel:[1,1,0] op_sel_hi:[1,1,0]
	v_fma_mix_f32 v24, v47, v47, v24 op_sel_hi:[1,1,0]
	v_fma_mix_f32 v25, v51, v51, v25 op_sel_hi:[1,1,0]
	v_fma_mix_f32 v26, v55, v55, v26 op_sel_hi:[1,1,0]
	v_fma_mix_f32 v27, v59, v59, v27 op_sel_hi:[1,1,0]
	v_fma_mix_f32 v24, v47, v47, v24 op_sel:[1,1,0] op_sel_hi:[1,1,0]
	v_fma_mix_f32 v25, v51, v51, v25 op_sel:[1,1,0] op_sel_hi:[1,1,0]
	v_fma_mix_f32 v26, v55, v55, v26 op_sel:[1,1,0] op_sel_hi:[1,1,0]
	v_fma_mix_f32 v27, v59, v59, v27 op_sel:[1,1,0] op_sel_hi:[1,1,0]
	s_waitcnt lgkmcnt(1)
	v_fma_mix_f32 v24, v60, v60, v24 op_sel_hi:[1,1,0]
	v_fma_mix_f32 v25, v64, v64, v25 op_sel_hi:[1,1,0]
	v_fma_mix_f32 v26, v68, v68, v26 op_sel_hi:[1,1,0]
	v_fma_mix_f32 v27, v72, v72, v27 op_sel_hi:[1,1,0]
	v_fma_mix_f32 v24, v60, v60, v24 op_sel:[1,1,0] op_sel_hi:[1,1,0]
	v_fma_mix_f32 v25, v64, v64, v25 op_sel:[1,1,0] op_sel_hi:[1,1,0]
	v_fma_mix_f32 v26, v68, v68, v26 op_sel:[1,1,0] op_sel_hi:[1,1,0]
	v_fma_mix_f32 v27, v72, v72, v27 op_sel:[1,1,0] op_sel_hi:[1,1,0]
	v_fma_mix_f32 v24, v61, v61, v24 op_sel_hi:[1,1,0]
	v_fma_mix_f32 v25, v65, v65, v25 op_sel_hi:[1,1,0]
	v_fma_mix_f32 v26, v69, v69, v26 op_sel_hi:[1,1,0]
	v_fma_mix_f32 v27, v73, v73, v27 op_sel_hi:[1,1,0]
	v_fma_mix_f32 v24, v61, v61, v24 op_sel:[1,1,0] op_sel_hi:[1,1,0]
	v_fma_mix_f32 v25, v65, v65, v25 op_sel:[1,1,0] op_sel_hi:[1,1,0]
	v_fma_mix_f32 v26, v69, v69, v26 op_sel:[1,1,0] op_sel_hi:[1,1,0]
	v_fma_mix_f32 v27, v73, v73, v27 op_sel:[1,1,0] op_sel_hi:[1,1,0]
	v_fma_mix_f32 v24, v62, v62, v24 op_sel_hi:[1,1,0]
	v_fma_mix_f32 v25, v66, v66, v25 op_sel_hi:[1,1,0]
	v_fma_mix_f32 v26, v70, v70, v26 op_sel_hi:[1,1,0]
	v_fma_mix_f32 v27, v74, v74, v27 op_sel_hi:[1,1,0]
	v_fma_mix_f32 v24, v62, v62, v24 op_sel:[1,1,0] op_sel_hi:[1,1,0]
	v_fma_mix_f32 v25, v66, v66, v25 op_sel:[1,1,0] op_sel_hi:[1,1,0]
	v_fma_mix_f32 v26, v70, v70, v26 op_sel:[1,1,0] op_sel_hi:[1,1,0]
	v_fma_mix_f32 v27, v74, v74, v27 op_sel:[1,1,0] op_sel_hi:[1,1,0]
	v_fma_mix_f32 v24, v63, v63, v24 op_sel_hi:[1,1,0]
	v_fma_mix_f32 v25, v67, v67, v25 op_sel_hi:[1,1,0]
	v_fma_mix_f32 v26, v71, v71, v26 op_sel_hi:[1,1,0]
	v_fma_mix_f32 v27, v75, v75, v27 op_sel_hi:[1,1,0]
	v_fma_mix_f32 v24, v63, v63, v24 op_sel:[1,1,0] op_sel_hi:[1,1,0]
	v_fma_mix_f32 v25, v67, v67, v25 op_sel:[1,1,0] op_sel_hi:[1,1,0]
	v_fma_mix_f32 v26, v71, v71, v26 op_sel:[1,1,0] op_sel_hi:[1,1,0]
	v_fma_mix_f32 v27, v75, v75, v27 op_sel:[1,1,0] op_sel_hi:[1,1,0]
	v_add_f32_e32 v24, v24, v25
	v_add_f32_e32 v26, v26, v27
	s_nop 0
	v_add_f32_e32 v24, v24, v26
	s_nop 0
	ds_max_u32 v20, v24
	s_waitcnt lgkmcnt(0)
	s_barrier
	s_and_saveexec_b64 s[2:3], s[0:1]
	s_cbranch_execz .LBB1_12
	v_lshlrev_b32_e32 v0, 2, v0
	v_add_u32_e32 v2, 0, v0
	v_add_u32_e32 v2, 0x20800, v2
	ds_read_b32 v2, v2
	s_lshl_b32 s0, s6, 5
	s_add_u32 s0, s16, s0
	s_addc_u32 s1, s17, 0
	s_waitcnt lgkmcnt(0)
	global_atomic_umax v0, v2, s[0:1]

	.amdhsa_kernel _Z11proj_kernelPKfS0_S0_PKDF16_S0_S0_S0_PDF16_S3_S3_Pj
		.amdhsa_group_segment_fixed_size 0
		.amdhsa_private_segment_fixed_size 0
		.amdhsa_kernarg_size 88
		.amdhsa_user_sgpr_count 2
		.amdhsa_user_sgpr_dispatch_ptr 0
		.amdhsa_user_sgpr_queue_ptr 0
		.amdhsa_user_sgpr_kernarg_segment_ptr 1
		.amdhsa_user_sgpr_dispatch_id 0
		.amdhsa_user_sgpr_kernarg_preload_length 0
		.amdhsa_user_sgpr_kernarg_preload_offset 0
		.amdhsa_user_sgpr_private_segment_size 0
		.amdhsa_uses_dynamic_stack 0
		.amdhsa_enable_private_segment 0
		.amdhsa_system_sgpr_workgroup_id_x 1
		.amdhsa_system_sgpr_workgroup_id_y 0
		.amdhsa_system_sgpr_workgroup_id_z 0
		.amdhsa_system_sgpr_workgroup_info 0
		.amdhsa_system_vgpr_workitem_id 0
		.amdhsa_next_free_vgpr 256
		.amdhsa_next_free_sgpr 64
		.amdhsa_accum_offset 256
		.amdhsa_reserve_vcc 1
		.amdhsa_float_round_mode_32 0
		.amdhsa_float_round_mode_16_64 0
		.amdhsa_float_denorm_mode_32 3
		.amdhsa_float_denorm_mode_16_64 3
		.amdhsa_dx10_clamp 1
		.amdhsa_ieee_mode 1
		.amdhsa_fp16_overflow 0
		.amdhsa_tg_split 0
		.amdhsa_exception_fp_ieee_invalid_op 0
		.amdhsa_exception_fp_denorm_src 0
		.amdhsa_exception_fp_ieee_div_zero 0
		.amdhsa_exception_fp_ieee_overflow 0
		.amdhsa_exception_fp_ieee_underflow 0
		.amdhsa_exception_fp_ieee_inexact 0
		.amdhsa_exception_int_div_zero 0
	.end_amdhsa_kernel

.Lattn_prio_done:
	s_add_u32 s38, s14, 0x6000
	s_addc_u32 s39, s15, 0
	s_add_u32 s40, s14, 0x8000
	s_addc_u32 s41, s15, 0
	s_add_u32 s42, s27, 0x2000
	s_addc_u32 s43, s28, 0
	s_and_b64 vcc, exec, s[16:17]
	s_cbranch_vccnz .Lattn_fast_loop

.Lattn_fast_loop:
	s_add_i32 s26, s26, 2
	v_add_u32_e32 v191, s3, v187
	ds_read_b64_tr_b16 v[176:177], v191 offset:24576
	ds_read_b64_tr_b16 v[178:179], v191 offset:25088
	s_waitcnt lgkmcnt(0)
	v_mfma_f32_32x32x16_f16 v[96:111], v[172:175], v[124:127], v[32:47]
	v_exp_f32_e32 v56, v56
	v_exp_f32_e32 v57, v57
	v_cvt_pk_f16_f32 v140, v64, v65
	v_cvt_pk_f16_f32 v141, v66, v67
	ds_read_b64_tr_b16 v[172:173], v191 offset:28672
	ds_read_b64_tr_b16 v[174:175], v191 offset:29184
	v_mfma_f32_32x32x16_f16 v[80:95], v[168:171], v[124:127], v[32:47]
	v_exp_f32_e32 v58, v58
	v_exp_f32_e32 v59, v59
	v_pk_add_f16 v128, v140, v141
	v_cvt_pk_f16_f32 v142, v68, v69
	v_cvt_pk_f16_f32 v143, v70, v71
	ds_read_b64_tr_b16 v[64:65], v191 offset:25600
	ds_read_b64_tr_b16 v[66:67], v191 offset:26112
	v_mfma_f32_32x32x16_f16 v[96:111], v[164:167], v[120:123], v[96:111]
	v_exp_f32_e32 v60, v60
	v_exp_f32_e32 v61, v61
	v_pk_add_f16 v129, v142, v143
	v_cvt_pk_f16_f32 v136, v72, v73
	v_cvt_pk_f16_f32 v137, v74, v75
	ds_read_b64_tr_b16 v[68:69], v191 offset:29696
	ds_read_b64_tr_b16 v[70:71], v191 offset:30208
	v_mfma_f32_32x32x16_f16 v[80:95], v[160:163], v[120:123], v[80:95]
	v_exp_f32_e32 v62, v62
	v_exp_f32_e32 v63, v63
	v_pk_add_f16 v72, v136, v137
	v_pk_add_f16 v128, v128, v129
	v_cvt_pk_f16_f32 v138, v76, v77
	v_cvt_pk_f16_f32 v139, v78, v79
	s_add_i32 m0, s31, s24
	s_min_u32 s2, s26, 28
	s_lshl_b32 s2, s2, 13
	s_add_u32 s2, s38, s2
	s_addc_u32 s3, s39, 0
	global_load_lds_dwordx4 v189, s[2:3]
	s_add_i32 m0, s29, s25
	ds_read_b64_tr_b16 v[76:77], v191 offset:26624
	ds_read_b64_tr_b16 v[78:79], v191 offset:27136
	v_mfma_f32_32x32x16_f16 v[96:111], v[156:159], v[116:119], v[96:111]
	v_pk_add_f16 v73, v138, v139
	v_cvt_pk_f16_f32 v132, v48, v49
	v_cvt_pk_f16_f32 v133, v50, v51
	ds_read_b64_tr_b16 v[48:49], v191 offset:30720
	ds_read_b64_tr_b16 v[50:51], v191 offset:31232
	v_mfma_f32_32x32x16_f16 v[80:95], v[152:155], v[116:119], v[80:95]
	v_pk_add_f16 v129, v72, v73
	v_cvt_pk_f16_f32 v134, v52, v53
	v_cvt_pk_f16_f32 v135, v54, v55
	v_pk_add_f16 v156, v132, v133
	global_load_lds_dwordx4 v189, s[42:43]
	ds_read_b64_tr_b16 v[72:73], v191 offset:27648
	ds_read_b64_tr_b16 v[74:75], v191 offset:28160
	v_mfma_f32_32x32x16_f16 v[96:111], v[148:151], v[112:115], v[96:111]
	v_pk_add_f16 v153, v128, v129
	v_cvt_pk_f16_f32 v128, v56, v57
	v_cvt_pk_f16_f32 v129, v58, v59
	v_pk_add_f16 v152, v134, v135
	ds_read_b64_tr_b16 v[52:53], v191 offset:31744
	ds_read_b64_tr_b16 v[54:55], v191 offset:32256
	v_mfma_f32_32x32x16_f16 v[80:95], v[144:147], v[112:115], v[80:95]
	v_pk_add_f16 v56, v128, v129
	v_pk_add_f16 v57, v156, v152
	v_cvt_pk_f16_f32 v130, v60, v61
	v_cvt_pk_f16_f32 v131, v62, v63
	v_pk_add_f16 v57, v153, v57
	v_pk_add_f16 v58, v130, v131
	v_mfma_f32_32x32x16_f16 v[0:15], v[140:143], v[176:179], v[0:15]
	v_exp_f32_e32 v96, v96
	v_exp_f32_e32 v97, v97
	v_exp_f32_e32 v98, v98
	v_pk_add_f16 v56, v56, v58
	s_nop 0
	v_pk_add_f16 v56, v57, v56
	s_nop 0
	v_cvt_f32_f16_e32 v57, v56
	v_cvt_f32_f16_sdwa v56, v56 dst_sel:DWORD dst_unused:UNUSED_PAD src0_sel:WORD_1
	v_add_f32_e32 v56, v56, v57
	v_add_f32_e32 v188, v56, v188
	s_waitcnt lgkmcnt(12)
	v_mfma_f32_32x32x16_f16 v[16:31], v[140:143], v[172:175], v[16:31]
	v_exp_f32_e32 v99, v99
	v_exp_f32_e32 v100, v100
	v_exp_f32_e32 v101, v101
	v_add_u32_e32 v60, s29, v190
	ds_read_b128 v[56:59], v60
	ds_read_b128 v[176:179], v60 offset:512
	s_waitcnt lgkmcnt(12)
	v_mfma_f32_32x32x16_f16 v[0:15], v[136:139], v[64:67], v[0:15]
	v_exp_f32_e32 v102, v102
	v_exp_f32_e32 v103, v103
	v_exp_f32_e32 v104, v104
	ds_read_b128 v[172:175], v60 offset:2048
	ds_read_b128 v[168:171], v60 offset:2560
	s_waitcnt lgkmcnt(12)
	v_mfma_f32_32x32x16_f16 v[16:31], v[136:139], v[68:71], v[16:31]
	v_exp_f32_e32 v105, v105
	v_exp_f32_e32 v106, v106
	v_exp_f32_e32 v107, v107
	ds_read_b128 v[164:167], v60 offset:4096
	ds_read_b128 v[160:163], v60 offset:4608
	s_waitcnt lgkmcnt(12)
	v_mfma_f32_32x32x16_f16 v[0:15], v[132:135], v[76:79], v[0:15]
	v_exp_f32_e32 v108, v108
	v_exp_f32_e32 v109, v109
	v_exp_f32_e32 v110, v110
	ds_read_b128 v[156:159], v60 offset:6144
	ds_read_b128 v[152:155], v60 offset:6656
	s_waitcnt lgkmcnt(12)
	v_mfma_f32_32x32x16_f16 v[16:31], v[132:135], v[48:51], v[16:31]
	v_exp_f32_e32 v111, v111
	v_exp_f32_e32 v80, v80
	v_exp_f32_e32 v81, v81
	s_waitcnt lgkmcnt(10)
	v_mfma_f32_32x32x16_f16 v[0:15], v[128:131], v[72:75], v[0:15]
	s_waitcnt vmcnt(2) lgkmcnt(0)
	s_barrier
	v_exp_f32_e32 v82, v82
	v_exp_f32_e32 v83, v83
	v_exp_f32_e32 v84, v84
	s_waitcnt lgkmcnt(8)
	v_mfma_f32_32x32x16_f16 v[16:31], v[128:131], v[52:55], v[16:31]
	v_exp_f32_e32 v85, v85
	v_exp_f32_e32 v86, v86
	v_exp_f32_e32 v87, v87
	s_add_i32 s33, s29, 0x2000
	s_cmpk_lg_i32 s29, 0x4000
	s_cselect_b32 s33, s33, 0
	v_add_u32_e32 v191, s31, v187
	ds_read_b64_tr_b16 v[148:149], v191 offset:24576
	ds_read_b64_tr_b16 v[150:151], v191 offset:25088
	s_waitcnt lgkmcnt(9)
	v_mfma_f32_32x32x16_f16 v[64:79], v[56:59], v[124:127], v[32:47]
	v_exp_f32_e32 v88, v88
	v_exp_f32_e32 v89, v89
	v_cvt_pk_f16_f32 v140, v96, v97
	v_cvt_pk_f16_f32 v141, v98, v99
	ds_read_b64_tr_b16 v[144:145], v191 offset:28672
	ds_read_b64_tr_b16 v[146:147], v191 offset:29184
	s_waitcnt lgkmcnt(10)
	v_mfma_f32_32x32x16_f16 v[48:63], v[176:179], v[124:127], v[32:47]
	v_exp_f32_e32 v90, v90
	v_exp_f32_e32 v91, v91
	v_pk_add_f16 v128, v140, v141
	v_cvt_pk_f16_f32 v142, v100, v101
	v_cvt_pk_f16_f32 v143, v102, v103
	ds_read_b64_tr_b16 v[96:97], v191 offset:25600
	ds_read_b64_tr_b16 v[98:99], v191 offset:26112
	s_waitcnt lgkmcnt(11)
	v_mfma_f32_32x32x16_f16 v[64:79], v[172:175], v[120:123], v[64:79]
	v_exp_f32_e32 v92, v92
	v_exp_f32_e32 v93, v93
	v_pk_add_f16 v129, v142, v143
	v_cvt_pk_f16_f32 v136, v104, v105
	v_cvt_pk_f16_f32 v137, v106, v107
	ds_read_b64_tr_b16 v[100:101], v191 offset:29696
	ds_read_b64_tr_b16 v[102:103], v191 offset:30208
	s_waitcnt lgkmcnt(12)
	v_mfma_f32_32x32x16_f16 v[48:63], v[168:171], v[120:123], v[48:63]
	v_exp_f32_e32 v94, v94
	v_exp_f32_e32 v95, v95
	v_pk_add_f16 v128, v128, v129
	v_cvt_pk_f16_f32 v138, v108, v109
	v_cvt_pk_f16_f32 v139, v110, v111
	v_pk_add_f16 v172, v136, v137
	s_add_i32 m0, s29, s24
	s_min_u32 s31, s26, 27
	s_lshl_b32 s31, s31, 13
	s_add_u32 s34, s40, s31
	s_addc_u32 s35, s41, 0
	global_load_lds_dwordx4 v189, s[34:35]
	s_add_i32 m0, s33, s25
	ds_read_b64_tr_b16 v[104:105], v191 offset:26624
	ds_read_b64_tr_b16 v[106:107], v191 offset:27136
	s_waitcnt lgkmcnt(13)
	v_mfma_f32_32x32x16_f16 v[64:79], v[164:167], v[116:119], v[64:79]
	v_pk_add_f16 v108, v138, v139
	v_cvt_pk_f16_f32 v132, v80, v81
	v_cvt_pk_f16_f32 v133, v82, v83
	ds_read_b64_tr_b16 v[80:81], v191 offset:30720
	ds_read_b64_tr_b16 v[82:83], v191 offset:31232
	s_waitcnt lgkmcnt(14)
	v_mfma_f32_32x32x16_f16 v[48:63], v[160:163], v[116:119], v[48:63]
	v_pk_add_f16 v129, v172, v108
	v_cvt_pk_f16_f32 v134, v84, v85
	v_cvt_pk_f16_f32 v135, v86, v87
	v_pk_add_f16 v164, v132, v133
	s_add_u32 s34, s42, 0x2000
	s_addc_u32 s35, s43, 0
	global_load_lds_dwordx4 v189, s[34:35]
	ds_read_b64_tr_b16 v[108:109], v191 offset:27648
	ds_read_b64_tr_b16 v[110:111], v191 offset:28160
	s_waitcnt lgkmcnt(14)
	v_mfma_f32_32x32x16_f16 v[64:79], v[156:159], v[112:115], v[64:79]
	v_pk_add_f16 v161, v128, v129
	v_cvt_pk_f16_f32 v128, v88, v89
	v_cvt_pk_f16_f32 v129, v90, v91
	v_pk_add_f16 v160, v134, v135
	ds_read_b64_tr_b16 v[84:85], v191 offset:31744
	ds_read_b64_tr_b16 v[86:87], v191 offset:32256
	v_mfma_f32_32x32x16_f16 v[48:63], v[152:155], v[112:115], v[48:63]
	v_pk_add_f16 v88, v128, v129
	v_pk_add_f16 v89, v164, v160
	v_cvt_pk_f16_f32 v130, v92, v93
	v_cvt_pk_f16_f32 v131, v94, v95
	v_pk_add_f16 v89, v161, v89
	v_pk_add_f16 v90, v130, v131
	s_waitcnt lgkmcnt(14)
	v_mfma_f32_32x32x16_f16 v[0:15], v[140:143], v[148:151], v[0:15]
	v_exp_f32_e32 v64, v64
	v_exp_f32_e32 v65, v65
	v_exp_f32_e32 v66, v66
	v_pk_add_f16 v88, v88, v90
	s_nop 0
	v_pk_add_f16 v88, v89, v88
	s_nop 0
	v_cvt_f32_f16_e32 v89, v88
	v_cvt_f32_f16_sdwa v88, v88 dst_sel:DWORD dst_unused:UNUSED_PAD src0_sel:WORD_1
	v_add_f32_e32 v88, v88, v89
	v_add_f32_e32 v188, v88, v188
	s_waitcnt lgkmcnt(12)
	v_mfma_f32_32x32x16_f16 v[16:31], v[140:143], v[144:147], v[16:31]
	v_exp_f32_e32 v67, v67
	v_exp_f32_e32 v68, v68
	v_exp_f32_e32 v69, v69
	v_add_u32_e32 v88, s33, v190
	ds_read_b128 v[172:175], v88
	ds_read_b128 v[168:171], v88 offset:512
	s_waitcnt lgkmcnt(12)
	v_mfma_f32_32x32x16_f16 v[0:15], v[136:139], v[96:99], v[0:15]
	v_exp_f32_e32 v70, v70
	v_exp_f32_e32 v71, v71
	v_exp_f32_e32 v72, v72
	ds_read_b128 v[164:167], v88 offset:2048
	ds_read_b128 v[160:163], v88 offset:2560
	s_waitcnt lgkmcnt(12)
	v_mfma_f32_32x32x16_f16 v[16:31], v[136:139], v[100:103], v[16:31]
	v_exp_f32_e32 v73, v73
	v_exp_f32_e32 v74, v74
	v_exp_f32_e32 v75, v75
	ds_read_b128 v[156:159], v88 offset:4096
	ds_read_b128 v[152:155], v88 offset:4608
	s_waitcnt lgkmcnt(12)
	v_mfma_f32_32x32x16_f16 v[0:15], v[132:135], v[104:107], v[0:15]
	v_exp_f32_e32 v76, v76
	v_exp_f32_e32 v77, v77
	v_exp_f32_e32 v78, v78
	ds_read_b128 v[148:151], v88 offset:6144
	ds_read_b128 v[144:147], v88 offset:6656
	s_waitcnt lgkmcnt(12)
	v_mfma_f32_32x32x16_f16 v[16:31], v[132:135], v[80:83], v[16:31]
	v_exp_f32_e32 v79, v79
	v_exp_f32_e32 v48, v48
	v_exp_f32_e32 v49, v49
	s_waitcnt lgkmcnt(10)
	v_mfma_f32_32x32x16_f16 v[0:15], v[128:131], v[108:111], v[0:15]
	s_waitcnt vmcnt(2) lgkmcnt(0)
	s_barrier
	v_exp_f32_e32 v50, v50
	v_exp_f32_e32 v51, v51
	v_exp_f32_e32 v52, v52
	s_waitcnt lgkmcnt(8)
	v_mfma_f32_32x32x16_f16 v[16:31], v[128:131], v[84:87], v[16:31]
	v_exp_f32_e32 v53, v53
	v_exp_f32_e32 v54, v54
	v_exp_f32_e32 v55, v55
	s_add_i32 s31, s33, 0x2000
	s_cmpk_lg_i32 s33, 0x4000
	s_cselect_b32 s34, s31, 0
	s_add_u32 s42, s42, 0x4000
	s_addc_u32 s43, s43, 0
	s_cmp_lt_u32 s26, 29
	s_cbranch_scc0 .Lattn_fast_exit
	s_mov_b32 s3, s29
	s_mov_b32 s31, s33
	s_mov_b32 s29, s34
	s_branch .Lattn_fast_loop
.Lattn_fast_exit:
	s_mov_b64 s[2:3], -1
	s_mov_b64 s[4:5], 0
	s_branch .LBB2_25

	.amdhsa_kernel _Z11attn_kernelPKDF16_S0_S0_PKjPf
		.amdhsa_group_segment_fixed_size 0
		.amdhsa_private_segment_fixed_size 0
		.amdhsa_kernarg_size 40
		.amdhsa_user_sgpr_count 2
		.amdhsa_user_sgpr_dispatch_ptr 0
		.amdhsa_user_sgpr_queue_ptr 0
		.amdhsa_user_sgpr_kernarg_segment_ptr 1
		.amdhsa_user_sgpr_dispatch_id 0
		.amdhsa_user_sgpr_kernarg_preload_length 0
		.amdhsa_user_sgpr_kernarg_preload_offset 0
		.amdhsa_user_sgpr_private_segment_size 0
		.amdhsa_uses_dynamic_stack 0
		.amdhsa_enable_private_segment 0
		.amdhsa_system_sgpr_workgroup_id_x 1
		.amdhsa_system_sgpr_workgroup_id_y 0
		.amdhsa_system_sgpr_workgroup_id_z 0
		.amdhsa_system_sgpr_workgroup_info 0
		.amdhsa_system_vgpr_workitem_id 0
		.amdhsa_next_free_vgpr 192
		.amdhsa_next_free_sgpr 44
		.amdhsa_accum_offset 192
		.amdhsa_reserve_vcc 1
		.amdhsa_float_round_mode_32 0
		.amdhsa_float_round_mode_16_64 0
		.amdhsa_float_denorm_mode_32 3
		.amdhsa_float_denorm_mode_16_64 3
		.amdhsa_dx10_clamp 1
		.amdhsa_ieee_mode 1
		.amdhsa_fp16_overflow 0
		.amdhsa_tg_split 0
		.amdhsa_exception_fp_ieee_invalid_op 0
		.amdhsa_exception_fp_denorm_src 0
		.amdhsa_exception_fp_ieee_div_zero 0
		.amdhsa_exception_fp_ieee_overflow 0
		.amdhsa_exception_fp_ieee_underflow 0
		.amdhsa_exception_fp_ieee_inexact 0
		.amdhsa_exception_int_div_zero 0
	.end_amdhsa_kernel

amdhsa.kernels:
  - .agpr_count:     0
    .args:
      - .actual_access:  read_only
        .address_space:  global
        .offset:         0
        .size:           8
        .value_kind:     global_buffer
      - .actual_access:  read_only
        .address_space:  global
        .offset:         8
        .size:           8
        .value_kind:     global_buffer
      - .actual_access:  read_only
        .address_space:  global
        .offset:         16
        .size:           8
        .value_kind:     global_buffer
      - .actual_access:  write_only
        .address_space:  global
        .offset:         24
        .size:           8
        .value_kind:     global_buffer
      - .actual_access:  write_only
        .address_space:  global
        .offset:         32
        .size:           8
        .value_kind:     global_buffer
    .group_segment_fixed_size: 0
    .kernarg_segment_align: 8
    .kernarg_segment_size: 40
    .language:       OpenCL C
    .language_version:
      - 2
      - 0
    .max_flat_workgroup_size: 256
    .name:           _Z12wprep_kernelPKfS0_S0_PDF16_Pj
    .private_segment_fixed_size: 0
    .sgpr_count:     18
    .sgpr_spill_count: 0
    .symbol:         _Z12wprep_kernelPKfS0_S0_PDF16_Pj.kd
    .uniform_work_group_size: 1
    .uses_dynamic_stack: false
    .vgpr_count:     12
    .vgpr_spill_count: 0
    .wavefront_size: 64
  - .agpr_count:     0
    .args:
      - .actual_access:  read_only
        .address_space:  global
        .offset:         0
        .size:           8
        .value_kind:     global_buffer
      - .actual_access:  read_only
        .address_space:  global
        .offset:         8
        .size:           8
        .value_kind:     global_buffer
      - .actual_access:  read_only
        .address_space:  global
        .offset:         16
        .size:           8
        .value_kind:     global_buffer
      - .actual_access:  read_only
        .address_space:  global
        .offset:         24
        .size:           8
        .value_kind:     global_buffer
      - .actual_access:  read_only
        .address_space:  global
        .offset:         32
        .size:           8
        .value_kind:     global_buffer
      - .actual_access:  read_only
        .address_space:  global
        .offset:         40
        .size:           8
        .value_kind:     global_buffer
      - .actual_access:  read_only
        .address_space:  global
        .offset:         48
        .size:           8
        .value_kind:     global_buffer
      - .actual_access:  write_only
        .address_space:  global
        .offset:         56
        .size:           8
        .value_kind:     global_buffer
      - .actual_access:  write_only
        .address_space:  global
        .offset:         64
        .size:           8
        .value_kind:     global_buffer
      - .actual_access:  write_only
        .address_space:  global
        .offset:         72
        .size:           8
        .value_kind:     global_buffer
      - .address_space:  global
        .offset:         80
        .size:           8
        .value_kind:     global_buffer
    .group_segment_fixed_size: 0
    .kernarg_segment_align: 8
    .kernarg_segment_size: 88
    .language:       OpenCL C
    .language_version:
      - 2
      - 0
    .max_flat_workgroup_size: 512
    .name:           _Z11proj_kernelPKfS0_S0_PKDF16_S0_S0_S0_PDF16_S3_S3_Pj
    .private_segment_fixed_size: 0
    .sgpr_count:     70
    .sgpr_spill_count: 0
    .symbol:         _Z11proj_kernelPKfS0_S0_PKDF16_S0_S0_S0_PDF16_S3_S3_Pj.kd
    .uniform_work_group_size: 1
    .uses_dynamic_stack: false
    .vgpr_count:     256
    .vgpr_spill_count: 0
    .wavefront_size: 64
  - .agpr_count:     0
    .args:
      - .actual_access:  read_only
        .address_space:  global
        .offset:         0
        .size:           8
        .value_kind:     global_buffer
      - .address_space:  global
        .offset:         8
        .size:           8
        .value_kind:     global_buffer
      - .address_space:  global
        .offset:         16
        .size:           8
        .value_kind:     global_buffer
      - .actual_access:  read_only
        .address_space:  global
        .offset:         24
        .size:           8
        .value_kind:     global_buffer
      - .actual_access:  write_only
        .address_space:  global
        .offset:         32
        .size:           8
        .value_kind:     global_buffer
    .group_segment_fixed_size: 0
    .kernarg_segment_align: 8
    .kernarg_segment_size: 40
    .language:       OpenCL C
    .language_version:
      - 2
      - 0
    .max_flat_workgroup_size: 512
    .name:           _Z11attn_kernelPKDF16_S0_S0_PKjPf
    .private_segment_fixed_size: 0
    .sgpr_count:     50
    .sgpr_spill_count: 0
    .symbol:         _Z11attn_kernelPKDF16_S0_S0_PKjPf.kd
    .uniform_work_group_size: 1
    .uses_dynamic_stack: false
    .vgpr_count:     192
    .vgpr_spill_count: 0
    .wavefront_size: 64
